# v60 plus gMLP unit: the tril(W) row pieces of all four k-steps loaded with the first one into spare VGPRs instead of one dependent round trip per conditional k-step block
# baseline (speedup 1.0000x reference)
.LBB0_366:
	s_andn2_b64 vcc, exec, s[2:3]
	s_mov_b64 s[2:3], -1
	s_cbranch_vccnz .LBB0_361
	s_ashr_i32 s2, s72, 7
	s_ashr_i32 s3, s2, 31
	s_lshl_b32 s70, s72, 4
	s_lshl_b64 s[2:3], s[2:3], 11
	s_and_b32 s70, s70, 0x780
	s_and_b32 s0, s72, 7
	s_or_b32 s2, s2, s70
	s_lshl_b32 s97, s0, 8
	v_lshl_add_u64 v[4:5], s[2:3], 0, v[80:81]
	v_mov_b64_e32 v[6:7], s[78:79]
	v_or_b32_e32 v8, s97, v88
	v_mad_u64_u32 v[6:7], s[70:71], v4, s33, v[6:7]
	v_mad_i32_i24 v7, v5, s33, v7
	v_lshlrev_b32_e32 v2, 1, v8
	v_lshl_add_u64 v[36:37], v[6:7], 0, v[2:3]
	s_movk_i32 s70, 0x5000
	v_add_co_u32_e32 v6, vcc, s70, v36
	s_mov_b32 s70, 0x65000
	s_nop 0
	v_addc_co_u32_e32 v7, vcc, 0, v37, vcc
	s_barrier
	global_load_dwordx4 v[20:23], v[6:7], off
	v_lshl_add_u64 v[38:39], v[4:5], 3, s[94:95]
	v_add_co_u32_e32 v4, vcc, s70, v36
	v_lshlrev_b32_e32 v2, 2, v8
	s_nop 0
	v_addc_co_u32_e32 v5, vcc, 0, v37, vcc
	global_load_dwordx4 v[24:27], v[4:5], off
	global_load_dwordx2 v[42:43], v[38:39], off
	global_load_dwordx2 v[34:35], v[38:39], off offset:128
	global_load_dwordx4 v[12:15], v2, s[84:85]
	global_load_dwordx4 v[16:19], v2, s[86:87]
	s_nop 0
	global_load_dwordx4 v[4:7], v2, s[84:85] offset:16
	global_load_dwordx4 v[8:11], v2, s[86:87] offset:16
	s_mov_b32 s70, 0xc5000
	v_add_co_u32_e32 v28, vcc, s70, v36
	global_load_dwordx2 v[44:45], v[38:39], off offset:256
	global_load_dwordx2 v[32:33], v[38:39], off offset:384
	global_load_dwordx2 v[40:41], v[38:39], off offset:512
	v_addc_co_u32_e32 v29, vcc, 0, v37, vcc
	global_load_dwordx4 v[46:49], v[28:29], off
	s_mov_b32 s71, 0x125000
	v_add_co_u32_e32 v28, vcc, s71, v36
	s_mov_b32 s70, 0x185000
	s_nop 0
	v_addc_co_u32_e32 v29, vcc, 0, v37, vcc
	global_load_dwordx4 v[28:31], v[28:29], off
	s_lshl_b32 s0, s0, 7
	v_cmp_ne_u32_e64 s[76:77], 1, v107
	s_waitcnt vmcnt(12)
	v_lshlrev_b32_e32 v2, 16, v20
	v_and_b32_e32 v20, 0xffff0000, v20
	v_lshlrev_b32_e32 v50, 16, v21
	v_and_b32_e32 v21, 0xffff0000, v21
	v_lshlrev_b32_e32 v51, 16, v22
	v_and_b32_e32 v22, 0xffff0000, v22
	s_waitcnt vmcnt(10)
	v_sub_f32_e32 v2, v2, v42
	v_sub_f32_e32 v20, v20, v42
	v_mul_f32_e32 v2, v43, v2
	v_mul_f32_e32 v20, v43, v20
	s_waitcnt vmcnt(7)
	v_fma_f32 v2, v12, v2, v16
	v_fma_f32 v20, v13, v20, v17
	v_lshlrev_b32_e32 v52, 16, v23
	v_and_b32_e32 v23, 0xffff0000, v23
	v_sub_f32_e32 v21, v21, v42
	v_cvt_pk_bf16_f32 v20, v2, v20
	v_and_b32_e32 v2, 0xffff0000, v24
	v_lshlrev_b32_e32 v53, 16, v24
	v_sub_f32_e32 v50, v50, v42
	v_sub_f32_e32 v22, v22, v42
	v_sub_f32_e32 v23, v23, v42
	v_mul_f32_e32 v21, v43, v21
	v_sub_f32_e32 v2, v2, v34
	v_sub_f32_e32 v51, v51, v42
	v_sub_f32_e32 v52, v52, v42
	v_sub_f32_e32 v42, v53, v34
	v_mul_f32_e32 v50, v43, v50
	v_mul_f32_e32 v22, v43, v22
	v_mul_f32_e32 v23, v43, v23
	v_fma_f32 v21, v15, v21, v19
	v_mul_f32_e32 v2, v35, v2
	v_mul_f32_e32 v51, v43, v51
	v_mul_f32_e32 v52, v43, v52
	v_mul_f32_e32 v42, v35, v42
	v_fma_f32 v43, v14, v50, v18
	s_waitcnt vmcnt(5)
	v_fma_f32 v22, v5, v22, v9
	v_fma_f32 v23, v7, v23, v11
	v_cvt_pk_bf16_f32 v21, v43, v21
	v_fma_f32 v2, v13, v2, v17
	v_fma_f32 v50, v4, v51, v8
	v_fma_f32 v51, v6, v52, v10
	v_fma_f32 v42, v12, v42, v16
	v_cvt_pk_bf16_f32 v22, v50, v22
	v_cvt_pk_bf16_f32 v23, v51, v23
	ds_write_b128 v106, v[20:23]
	v_cvt_pk_bf16_f32 v20, v42, v2
	v_lshlrev_b32_e32 v2, 16, v25
	v_and_b32_e32 v21, 0xffff0000, v25
	v_sub_f32_e32 v2, v2, v34
	v_sub_f32_e32 v21, v21, v34
	v_mul_f32_e32 v2, v35, v2
	v_mul_f32_e32 v21, v35, v21
	v_fma_f32 v2, v14, v2, v18
	v_fma_f32 v21, v15, v21, v19
	v_cvt_pk_bf16_f32 v21, v2, v21
	v_lshlrev_b32_e32 v2, 16, v26
	v_and_b32_e32 v22, 0xffff0000, v26
	v_sub_f32_e32 v2, v2, v34
	v_sub_f32_e32 v22, v22, v34
	v_mul_f32_e32 v2, v35, v2
	v_mul_f32_e32 v22, v35, v22
	v_fma_f32 v2, v4, v2, v8
	v_fma_f32 v22, v5, v22, v9
	v_and_b32_e32 v23, 0xffff0000, v27
	v_cvt_pk_bf16_f32 v22, v2, v22
	v_lshlrev_b32_e32 v2, 16, v27
	v_sub_f32_e32 v23, v23, v34
	v_sub_f32_e32 v2, v2, v34
	v_mul_f32_e32 v23, v35, v23
	v_mul_f32_e32 v2, v35, v2
	v_fma_f32 v23, v7, v23, v11
	v_fma_f32 v2, v6, v2, v10
	v_cvt_pk_bf16_f32 v23, v2, v23
	ds_write_b128 v106, v[20:23] offset:4096
	v_add_co_u32_e32 v20, vcc, s70, v36
	s_waitcnt vmcnt(1)
	v_lshlrev_b32_e32 v2, 16, v46
	v_addc_co_u32_e32 v21, vcc, 0, v37, vcc
	global_load_dwordx4 v[20:23], v[20:21], off
	v_and_b32_e32 v24, 0xffff0000, v46
	v_sub_f32_e32 v2, v2, v44
	v_sub_f32_e32 v24, v24, v44
	v_mul_f32_e32 v2, v45, v2
	v_mul_f32_e32 v24, v45, v24
	v_fma_f32 v2, v12, v2, v16
	v_fma_f32 v24, v13, v24, v17
	v_cvt_pk_bf16_f32 v24, v2, v24
	v_lshlrev_b32_e32 v2, 16, v47
	v_and_b32_e32 v25, 0xffff0000, v47
	v_sub_f32_e32 v2, v2, v44
	v_sub_f32_e32 v25, v25, v44
	v_mul_f32_e32 v2, v45, v2
	v_mul_f32_e32 v25, v45, v25
	v_fma_f32 v2, v14, v2, v18
	v_fma_f32 v25, v15, v25, v19
	v_cvt_pk_bf16_f32 v25, v2, v25
	v_lshlrev_b32_e32 v2, 16, v48
	v_and_b32_e32 v26, 0xffff0000, v48
	v_sub_f32_e32 v2, v2, v44
	v_sub_f32_e32 v26, v26, v44
	v_mul_f32_e32 v2, v45, v2
	v_mul_f32_e32 v26, v45, v26
	v_fma_f32 v2, v4, v2, v8
	v_fma_f32 v26, v5, v26, v9
	v_and_b32_e32 v27, 0xffff0000, v49
	v_cvt_pk_bf16_f32 v26, v2, v26
	v_lshlrev_b32_e32 v2, 16, v49
	v_sub_f32_e32 v27, v27, v44
	v_sub_f32_e32 v2, v2, v44
	v_mul_f32_e32 v27, v45, v27
	v_mul_f32_e32 v2, v45, v2
	v_fma_f32 v27, v7, v27, v11
	v_fma_f32 v2, v6, v2, v10
	v_cvt_pk_bf16_f32 v27, v2, v27
	ds_write_b128 v106, v[24:27] offset:8192
	s_waitcnt vmcnt(1)
	v_and_b32_e32 v24, 0xffff0000, v28
	v_lshlrev_b32_e32 v2, 16, v28
	v_sub_f32_e32 v24, v24, v32
	v_sub_f32_e32 v2, v2, v32
	v_mul_f32_e32 v24, v33, v24
	v_mul_f32_e32 v2, v33, v2
	v_fma_f32 v24, v13, v24, v17
	s_mov_b32 s70, 0x1e5000
	v_fma_f32 v2, v12, v2, v16
	v_cvt_pk_bf16_f32 v28, v2, v24
	v_add_co_u32_e32 v24, vcc, s70, v36
	v_lshlrev_b32_e32 v2, 16, v29
	s_nop 0
	v_addc_co_u32_e32 v25, vcc, 0, v37, vcc
	global_load_dwordx4 v[24:27], v[24:25], off
	s_nop 0
	global_load_dwordx2 v[42:43], v[38:39], off offset:640
	v_and_b32_e32 v29, 0xffff0000, v29
	v_sub_f32_e32 v2, v2, v32
	v_sub_f32_e32 v29, v29, v32
	v_mul_f32_e32 v2, v33, v2
	v_mul_f32_e32 v29, v33, v29
	v_fma_f32 v2, v14, v2, v18
	v_fma_f32 v29, v15, v29, v19
	v_cvt_pk_bf16_f32 v29, v2, v29
	v_lshlrev_b32_e32 v2, 16, v30
	v_and_b32_e32 v30, 0xffff0000, v30
	v_sub_f32_e32 v2, v2, v32
	v_sub_f32_e32 v30, v30, v32
	v_mul_f32_e32 v2, v33, v2
	v_mul_f32_e32 v30, v33, v30
	v_fma_f32 v2, v4, v2, v8
	v_fma_f32 v30, v5, v30, v9
	v_cvt_pk_bf16_f32 v30, v2, v30
	v_lshlrev_b32_e32 v2, 16, v31
	v_and_b32_e32 v31, 0xffff0000, v31
	v_sub_f32_e32 v31, v31, v32
	v_sub_f32_e32 v2, v2, v32
	v_mul_f32_e32 v31, v33, v31
	v_mul_f32_e32 v2, v33, v2
	v_fma_f32 v31, v7, v31, v11
	s_mov_b32 s70, 0x245000
	v_fma_f32 v2, v6, v2, v10
	v_cvt_pk_bf16_f32 v31, v2, v31
	ds_write_b128 v106, v[28:31] offset:12288
	v_add_co_u32_e32 v28, vcc, s70, v36
	s_waitcnt vmcnt(2)
	v_lshlrev_b32_e32 v2, 16, v20
	v_addc_co_u32_e32 v29, vcc, 0, v37, vcc
	global_load_dwordx4 v[28:31], v[28:29], off
	s_nop 0
	global_load_dwordx2 v[44:45], v[38:39], off offset:768
	v_and_b32_e32 v20, 0xffff0000, v20
	v_sub_f32_e32 v20, v20, v40
	v_sub_f32_e32 v2, v2, v40
	v_mul_f32_e32 v20, v41, v20
	v_mul_f32_e32 v2, v41, v2
	v_fma_f32 v20, v13, v20, v17
	v_fma_f32 v2, v12, v2, v16
	v_cvt_pk_bf16_f32 v32, v2, v20
	v_and_b32_e32 v20, 0xffff0000, v21
	v_lshlrev_b32_e32 v2, 16, v21
	v_sub_f32_e32 v20, v20, v40
	v_sub_f32_e32 v2, v2, v40
	v_mul_f32_e32 v20, v41, v20
	v_mul_f32_e32 v2, v41, v2
	v_fma_f32 v20, v15, v20, v19
	v_fma_f32 v2, v14, v2, v18
	v_cvt_pk_bf16_f32 v33, v2, v20
	v_and_b32_e32 v20, 0xffff0000, v22
	v_lshlrev_b32_e32 v2, 16, v22
	v_sub_f32_e32 v20, v20, v40
	v_sub_f32_e32 v2, v2, v40
	v_mul_f32_e32 v20, v41, v20
	v_mul_f32_e32 v2, v41, v2
	v_fma_f32 v20, v5, v20, v9
	v_fma_f32 v2, v4, v2, v8
	v_cvt_pk_bf16_f32 v34, v2, v20
	v_and_b32_e32 v20, 0xffff0000, v23
	s_mov_b32 s70, 0x2a5000
	v_sub_f32_e32 v35, v20, v40
	v_add_co_u32_e32 v20, vcc, s70, v36
	v_lshlrev_b32_e32 v2, 16, v23
	s_nop 0
	v_addc_co_u32_e32 v21, vcc, 0, v37, vcc
	global_load_dwordx4 v[20:23], v[20:21], off
	s_nop 0
	global_load_dwordx2 v[36:37], v[38:39], off offset:896
	v_sub_f32_e32 v2, v2, v40
	v_mul_f32_e32 v2, v41, v2
	v_mul_f32_e32 v35, v41, v35
	v_fma_f32 v2, v6, v2, v10
	v_fma_f32 v35, v7, v35, v11
	v_cvt_pk_bf16_f32 v35, v2, v35
	s_andn2_b64 vcc, exec, s[88:89]
	ds_write_b128 v106, v[32:35] offset:16384
	s_waitcnt vmcnt(5)
	v_lshlrev_b32_e32 v2, 16, v24
	v_and_b32_e32 v24, 0xffff0000, v24
	s_waitcnt vmcnt(4)
	v_sub_f32_e32 v2, v2, v42
	v_sub_f32_e32 v24, v24, v42
	v_mul_f32_e32 v2, v43, v2
	v_mul_f32_e32 v24, v43, v24
	v_fma_f32 v2, v12, v2, v16
	v_fma_f32 v24, v13, v24, v17
	v_cvt_pk_bf16_f32 v24, v2, v24
	v_lshlrev_b32_e32 v2, 16, v25
	v_and_b32_e32 v25, 0xffff0000, v25
	v_sub_f32_e32 v2, v2, v42
	v_sub_f32_e32 v25, v25, v42
	v_mul_f32_e32 v2, v43, v2
	v_mul_f32_e32 v25, v43, v25
	v_fma_f32 v2, v14, v2, v18
	v_fma_f32 v25, v15, v25, v19
	v_cvt_pk_bf16_f32 v25, v2, v25
	v_lshlrev_b32_e32 v2, 16, v26
	v_and_b32_e32 v26, 0xffff0000, v26
	v_sub_f32_e32 v2, v2, v42
	v_sub_f32_e32 v26, v26, v42
	v_mul_f32_e32 v2, v43, v2
	v_mul_f32_e32 v26, v43, v26
	v_fma_f32 v2, v4, v2, v8
	v_fma_f32 v26, v5, v26, v9
	v_cvt_pk_bf16_f32 v26, v2, v26
	v_lshlrev_b32_e32 v2, 16, v27
	v_and_b32_e32 v27, 0xffff0000, v27
	v_sub_f32_e32 v2, v2, v42
	v_sub_f32_e32 v27, v27, v42
	v_mul_f32_e32 v2, v43, v2
	v_mul_f32_e32 v27, v43, v27
	v_fma_f32 v2, v6, v2, v10
	v_fma_f32 v27, v7, v27, v11
	v_cvt_pk_bf16_f32 v27, v2, v27
	ds_write_b128 v106, v[24:27] offset:20480
	s_waitcnt vmcnt(3)
	v_lshlrev_b32_e32 v2, 16, v28
	v_and_b32_e32 v24, 0xffff0000, v28
	s_waitcnt vmcnt(2)
	v_sub_f32_e32 v2, v2, v44
	v_sub_f32_e32 v24, v24, v44
	v_mul_f32_e32 v2, v45, v2
	v_mul_f32_e32 v24, v45, v24
	v_fma_f32 v2, v12, v2, v16
	v_fma_f32 v24, v13, v24, v17
	v_cvt_pk_bf16_f32 v24, v2, v24
	v_lshlrev_b32_e32 v2, 16, v29
	v_and_b32_e32 v25, 0xffff0000, v29
	v_sub_f32_e32 v2, v2, v44
	v_sub_f32_e32 v25, v25, v44
	v_mul_f32_e32 v2, v45, v2
	v_mul_f32_e32 v25, v45, v25
	v_fma_f32 v2, v14, v2, v18
	v_fma_f32 v25, v15, v25, v19
	v_cvt_pk_bf16_f32 v25, v2, v25
	v_lshlrev_b32_e32 v2, 16, v30
	v_and_b32_e32 v26, 0xffff0000, v30
	v_sub_f32_e32 v2, v2, v44
	v_sub_f32_e32 v26, v26, v44
	v_mul_f32_e32 v2, v45, v2
	v_mul_f32_e32 v26, v45, v26
	v_fma_f32 v2, v4, v2, v8
	v_fma_f32 v26, v5, v26, v9
	v_cvt_pk_bf16_f32 v26, v2, v26
	v_lshlrev_b32_e32 v2, 16, v31
	v_and_b32_e32 v27, 0xffff0000, v31
	v_sub_f32_e32 v2, v2, v44
	v_sub_f32_e32 v27, v27, v44
	v_mul_f32_e32 v2, v45, v2
	v_mul_f32_e32 v27, v45, v27
	v_fma_f32 v2, v6, v2, v10
	v_fma_f32 v27, v7, v27, v11
	v_cvt_pk_bf16_f32 v27, v2, v27
	s_waitcnt vmcnt(1)
	v_lshlrev_b32_e32 v2, 16, v20
	s_waitcnt vmcnt(0)
	v_sub_f32_e32 v2, v2, v36
	v_mul_f32_e32 v2, v37, v2
	v_fma_f32 v2, v12, v2, v16
	v_and_b32_e32 v12, 0xffff0000, v20
	v_sub_f32_e32 v12, v12, v36
	v_mul_f32_e32 v12, v37, v12
	v_fma_f32 v12, v13, v12, v17
	v_cvt_pk_bf16_f32 v12, v2, v12
	v_lshlrev_b32_e32 v2, 16, v21
	v_sub_f32_e32 v2, v2, v36
	v_and_b32_e32 v13, 0xffff0000, v21
	v_mul_f32_e32 v2, v37, v2
	v_sub_f32_e32 v13, v13, v36
	v_fma_f32 v2, v14, v2, v18
	v_mul_f32_e32 v13, v37, v13
	v_fmac_f32_e32 v19, v15, v13
	v_cvt_pk_bf16_f32 v13, v2, v19
	v_lshlrev_b32_e32 v2, 16, v22
	v_sub_f32_e32 v2, v2, v36
	v_mul_f32_e32 v2, v37, v2
	v_fma_f32 v2, v4, v2, v8
	v_and_b32_e32 v4, 0xffff0000, v22
	v_sub_f32_e32 v4, v4, v36
	v_mul_f32_e32 v4, v37, v4
	v_fma_f32 v4, v5, v4, v9
	v_cvt_pk_bf16_f32 v14, v2, v4
	v_and_b32_e32 v4, 0xffff0000, v23
	v_sub_f32_e32 v4, v4, v36
	v_mul_f32_e32 v4, v37, v4
	v_lshlrev_b32_e32 v2, 16, v23
	v_fmac_f32_e32 v11, v7, v4
	v_lshl_add_u64 v[4:5], s[0:1], 0, v[82:83]
	v_sub_f32_e32 v2, v2, v36
	v_lshlrev_b64 v[4:5], 9, v[4:5]
	v_mul_f32_e32 v2, v37, v2
	v_lshl_add_u64 v[8:9], v[84:85], 0, v[4:5]
	ds_write_b128 v106, v[24:27] offset:24576
	v_fma_f32 v2, v6, v2, v10
	v_cvt_pk_bf16_f32 v15, v2, v11
	ds_write_b128 v106, v[12:15] offset:28672
	s_cbranch_vccnz .LBB0_372
	global_load_dwordx4 v[4:7], v[8:9], off
	global_load_dwordx4 v[10:13], v[8:9], off offset:16
	global_load_dwordx4 v[200:203], v[8:9], off offset:128
	global_load_dwordx4 v[204:207], v[8:9], off offset:144
	global_load_dwordx4 v[208:211], v[8:9], off offset:256
	global_load_dwordx4 v[212:215], v[8:9], off offset:272
	global_load_dwordx4 v[216:219], v[8:9], off offset:384
	global_load_dwordx4 v[220:223], v[8:9], off offset:400
	v_readlane_b32 s70, v255, 22
	v_readlane_b32 s71, v255, 23
	s_waitcnt vmcnt(7)
	s_nop 0
	v_cndmask_b32_e64 v2, v4, 0, s[70:71]
	v_readlane_b32 s70, v255, 24
	v_readlane_b32 s71, v255, 25
	s_nop 1
	v_cndmask_b32_e64 v4, 0, v5, s[70:71]
	v_readlane_b32 s70, v255, 26
	v_readlane_b32 s71, v255, 27
	v_cvt_pk_bf16_f32 v4, v2, v4
	s_nop 1
	v_cndmask_b32_e64 v5, v6, 0, s[70:71]
	v_cndmask_b32_e64 v6, v7, 0, s[10:11]
	s_waitcnt vmcnt(6)
	v_cndmask_b32_e64 v7, v10, 0, s[12:13]
	v_cndmask_b32_e64 v10, v11, 0, s[14:15]
	v_cndmask_b32_e64 v11, v12, 0, s[16:17]
	v_cndmask_b32_e64 v12, v13, 0, s[18:19]
	v_cvt_pk_bf16_f32 v5, v5, v6
	v_cvt_pk_bf16_f32 v6, v7, v10
	v_cvt_pk_bf16_f32 v7, v11, v12
	v_cndmask_b32_e64 v2, 0, 1, s[4:5]
	v_cmp_ne_u32_e64 s[74:75], 1, v2
	s_andn2_b64 vcc, exec, s[4:5]
	s_cbranch_vccz .LBB0_373

.LBB0_373:
	s_waitcnt vmcnt(4)
	v_mov_b64_e32 v[10:11], v[200:201]
	v_mov_b64_e32 v[12:13], v[202:203]
	v_mov_b64_e32 v[14:15], v[204:205]
	v_mov_b64_e32 v[16:17], v[206:207]
	v_cndmask_b32_e64 v2, v10, 0, s[20:21]
	v_cndmask_b32_e64 v10, 0, v11, s[22:23]
	v_cndmask_b32_e64 v11, v12, 0, s[24:25]
	v_cndmask_b32_e64 v12, v13, 0, s[26:27]
	v_cndmask_b32_e64 v13, v14, 0, s[28:29]
	v_cndmask_b32_e64 v14, v15, 0, s[30:31]
	v_cndmask_b32_e64 v15, v16, 0, s[34:35]
	v_cndmask_b32_e64 v16, v17, 0, s[36:37]
	v_cvt_pk_bf16_f32 v76, v2, v10
	v_cvt_pk_bf16_f32 v77, v11, v12
	v_cvt_pk_bf16_f32 v78, v13, v14
	v_cvt_pk_bf16_f32 v79, v15, v16
	v_cndmask_b32_e64 v2, 0, 1, s[6:7]
	v_cmp_ne_u32_e64 s[72:73], 1, v2
	s_andn2_b64 vcc, exec, s[6:7]
	s_cbranch_vccnz .LBB0_370
.LBB0_374:
	s_waitcnt vmcnt(2)
	v_mov_b64_e32 v[10:11], v[208:209]
	v_mov_b64_e32 v[12:13], v[210:211]
	v_mov_b64_e32 v[14:15], v[212:213]
	v_mov_b64_e32 v[16:17], v[214:215]
	v_cndmask_b32_e64 v2, v10, 0, s[38:39]
	v_cndmask_b32_e64 v10, 0, v11, s[40:41]
	v_cndmask_b32_e64 v11, v12, 0, s[42:43]
	v_cndmask_b32_e64 v12, v13, 0, s[44:45]
	v_cndmask_b32_e64 v13, v14, 0, s[46:47]
	v_cndmask_b32_e64 v14, v15, 0, s[48:49]
	v_cndmask_b32_e64 v15, v16, 0, s[50:51]
	v_cndmask_b32_e64 v16, v17, 0, s[52:53]
	v_cvt_pk_bf16_f32 v72, v2, v10
	v_cvt_pk_bf16_f32 v73, v11, v12
	v_cvt_pk_bf16_f32 v74, v13, v14
	v_cvt_pk_bf16_f32 v75, v15, v16
	v_cndmask_b32_e64 v2, 0, 1, s[8:9]
	v_cmp_ne_u32_e64 s[70:71], 1, v2
	s_andn2_b64 vcc, exec, s[8:9]
	s_cbranch_vccnz .LBB0_371
.LBB0_375:
	s_waitcnt vmcnt(0)
	v_mov_b64_e32 v[10:11], v[216:217]
	v_mov_b64_e32 v[12:13], v[218:219]
	v_mov_b64_e32 v[14:15], v[220:221]
	v_mov_b64_e32 v[16:17], v[222:223]
	v_cndmask_b32_e64 v2, v10, 0, s[54:55]
	v_cndmask_b32_e64 v8, 0, v11, s[56:57]
	v_cndmask_b32_e64 v9, v12, 0, s[58:59]
	v_cndmask_b32_e64 v10, v13, 0, s[60:61]
	v_cndmask_b32_e64 v11, v14, 0, s[62:63]
	v_cndmask_b32_e64 v12, v15, 0, s[64:65]
	v_cndmask_b32_e64 v13, v16, 0, s[66:67]
	v_cndmask_b32_e64 v14, v17, 0, s[68:69]
	v_cvt_pk_bf16_f32 v68, v2, v8
	v_cvt_pk_bf16_f32 v69, v9, v10
	v_cvt_pk_bf16_f32 v70, v11, v12
	v_cvt_pk_bf16_f32 v71, v13, v14
